# prep: hidden-half tiles (longer second stage) assigned to the first-dispatched 128 blocks, encoder-half tiles to the last 128; rest as v40
# speedup vs baseline: 1.0011x; 1.0011x over previous
_Z11prep_kernelPKfS0_S0_S0_Pf:
	s_load_dwordx8 s[4:11], s[0:1], 0x0
	s_load_dwordx2 s[12:13], s[0:1], 0x20
	s_cmpk_eq_i32 s2, 0x100
	s_cbranch_scc1 .Lprep_exit
	s_and_b32 s14, s2, 31
	s_lshr_b32 s15, s2, 7
	s_lshl_b32 s15, s15, 5
	s_or_b32 s14, s14, s15
	s_bfe_u32 s15, s2, 0x20005
	v_and_b32_e32 v1, 7, v0
	v_and_b32_e32 v2, 0x3f8, v0
	v_lshlrev_b32_e32 v3, 10, v2
	v_lshl_or_b32 v3, v1, 4, v3
	s_lshl_b32 s16, s15, 21
	s_lshl_b32 s17, s14, 7
	s_add_i32 s16, s16, s17
	v_add_u32_e32 v3, s16, v3
	v_add_u32_e32 v4, 0x100000, v3
	v_lshrrev_b32_e32 v5, 1, v2
	s_lshl_b32 s18, s15, 10
	v_add_u32_e32 v5, s18, v5
	v_and_b32_e32 v19, 63, v0
	v_lshrrev_b32_e32 v20, 6, v0
	s_waitcnt lgkmcnt(0)
	global_load_dwordx4 v[8:11], v3, s[4:5] nt
	global_load_dwordx4 v[12:15], v4, s[4:5] nt
	global_load_dword v6, v5, s[6:7]
	global_load_dword v16, v5, s[6:7] offset:512
	s_cmp_lt_u32 s14, 32
	s_cbranch_scc0 .Lprep_ld_done
	v_cmp_gt_u32_e32 vcc, 0x200, v0
	s_and_saveexec_b64 s[20:21], vcc
	s_cbranch_execz .Lprep_hb_skip
	v_lshrrev_b32_e32 v17, 5, v0
	v_and_b32_e32 v18, 31, v0
	v_lshlrev_b32_e32 v17, 12, v17
	v_lshl_or_b32 v17, v18, 2, v17
	v_add_u32_e32 v17, s17, v17
	global_load_dword v36, v17, s[10:11]
